# attention loop: K/V ring slot indices (mod 3, mod 4) carried in spare SGPRs and rotated once per iteration instead of recomputed at each of 11 sites (18 fewer scalar instructions per iteration)
# speedup vs baseline: 1.0034x; 1.0034x over previous
.LBB0_1317:
	v_add_f32_e32 v193, 0, v154
	s_or_b32 s44, s60, 1
	s_cmp_ge_i32 s44, s71
	s_cbranch_scc1 .LBB0_1360
	s_and_b64 s[52:53], s[52:53], exec
	s_cselect_b32 s60, 3, 2
	s_ashr_i32 s45, s44, 31
	s_lshl_b64 s[52:53], s[44:45], 17
	s_add_u32 s45, s52, s46
	s_addc_u32 s59, s53, s47
	s_lshl_b64 s[52:53], s[54:55], 1
	s_add_u32 s52, s45, s52
	s_addc_u32 s53, s59, s53
	s_lshl_b32 s45, s24, 15
	s_and_b32 s45, s45, 0x18000
	v_lshl_add_u32 v66, s58, 6, v246
	v_lshl_or_b32 v166, v247, 1, s45
	v_subrev_u32_e32 v195, s75, v66
	v_lshl_add_u64 v[66:67], s[52:53], 0, v[166:167]
	s_add_i32 s52, s16, s73
	s_add_i32 s54, s58, 4
	s_ashr_i32 s53, s52, 31
	s_ashr_i32 s55, s54, 31
	s_lshl_b64 s[52:53], s[52:53], 18
	s_lshl_b64 s[58:59], s[54:55], 11
	s_add_u32 s45, s52, s58
	s_addc_u32 s53, s53, s59
	s_and_b32 s52, s74, 16
	s_or_b32 s52, s45, s52
	v_lshl_add_u64 v[220:221], v[188:189], 0, s[52:53]
	s_lshl_b64 s[52:53], s[54:55], 17
	s_add_u32 s45, s52, s46
	s_addc_u32 s52, s53, s47
	s_lshl_b64 s[50:51], s[50:51], 1
	s_add_u32 s50, s45, s50
	s_addc_u32 s51, s52, s51
	v_lshl_add_u64 v[218:219], v[208:209], 0, v[66:67]
	v_lshl_add_u64 v[222:223], v[210:211], 0, s[50:51]
	s_mov_b32 s100, m0
	s_add_i32 s93, s44, -2
	s_mul_hi_i32 s90, s93, 0x55555556
	s_mul_i32 s90, s90, 3
	s_sub_i32 s90, s93, s90
	s_mul_hi_i32 s91, s44, 0x55555556
	s_mul_i32 s91, s91, 3
	s_sub_i32 s91, s44, s91
	s_add_i32 s92, s90, s91
	s_sub_i32 s92, 3, s92
	s_add_i32 s98, s44, -1
	s_and_b32 s98, s98, 3
	s_mulk_i32 s98, 0x2800
	s_and_b32 s99, s44, 3
	s_mulk_i32 s99, 0x2800
.LBB0_1319:
	v_mfma_f32_32x32x16_bf16 v[82:97], v[138:141], v[98:101], 0
	v_lshl_add_u32 v162, s90, 13, v240
	ds_read_b64_tr_b16 v[142:143], v162 offset:40960
	ds_read_b64_tr_b16 v[144:145], v162 offset:41472
	s_add_i32 s45, s44, -1
	v_add_f32_e32 v66, v50, v51
	v_add_f32_e32 v67, v52, v53
	v_add_f32_e32 v66, v66, v67
	v_cvt_pk_bf16_f32 v138, v50, v51
	v_cvt_pk_bf16_f32 v139, v52, v53
	ds_read_b64_tr_b16 v[146:147], v162 offset:45056
	ds_read_b64_tr_b16 v[148:149], v162 offset:45568
	v_add_f32_e32 v50, v54, v55
	v_add_f32_e32 v51, v56, v57
	v_add_f32_e32 v50, v50, v51
	v_add_f32_e32 v50, v50, v66
	v_mfma_f32_32x32x16_bf16 v[66:81], v[130:133], v[98:101], 0
	v_cvt_pk_bf16_f32 v140, v54, v55
	v_cvt_pk_bf16_f32 v141, v56, v57
	v_add_u32_e32 v150, s98, v238
	ds_read_b128 v[130:133], v150 offset:6144
	ds_read_b128 v[158:161], v150 offset:6656
	ds_read_b64_tr_b16 v[54:55], v162 offset:41984
	ds_read_b64_tr_b16 v[56:57], v162 offset:42496
	v_mfma_f32_32x32x16_bf16 v[82:97], v[134:137], v[102:105], v[82:97]
	v_add_f32_e32 v51, v58, v59
	v_add_f32_e32 v52, v60, v61
	v_add_f32_e32 v51, v51, v52
	v_add_f32_e32 v52, v51, v50
	v_cvt_pk_bf16_f32 v50, v58, v59
	v_cvt_pk_bf16_f32 v51, v60, v61
	ds_read_b64_tr_b16 v[58:59], v162 offset:46080
	ds_read_b64_tr_b16 v[60:61], v162 offset:46592
	v_mfma_f32_32x32x16_bf16 v[66:81], v[126:129], v[102:105], v[66:81]
	v_add_f32_e32 v53, v62, v63
	v_add_f32_e32 v126, v64, v65
	v_add_f32_e32 v53, v53, v126
	v_add_f32_e32 v151, v53, v52
	v_cvt_pk_bf16_f32 v52, v62, v63
	v_cvt_pk_bf16_f32 v53, v64, v65
	ds_read_b128 v[126:129], v150 offset:8192
	ds_read_b128 v[134:137], v150 offset:8704
	ds_read_b64_tr_b16 v[62:63], v162 offset:43008
	ds_read_b64_tr_b16 v[64:65], v162 offset:43520
	v_mfma_f32_32x32x16_bf16 v[82:97], v[122:125], v[106:109], v[82:97]
	v_add_f32_e32 v122, v34, v35
	v_add_f32_e32 v123, v36, v37
	v_add_f32_e32 v122, v122, v123
	v_add_f32_e32 v122, v122, v151
	v_cvt_pk_bf16_f32 v34, v34, v35
	v_cvt_pk_bf16_f32 v35, v36, v37
	ds_read_b64_tr_b16 v[150:151], v162 offset:47104
	ds_read_b64_tr_b16 v[152:153], v162 offset:47616
	v_mfma_f32_32x32x16_bf16 v[66:81], v[118:121], v[106:109], v[66:81]
	v_add_f32_e32 v36, v38, v39
	v_add_f32_e32 v37, v40, v41
	v_add_f32_e32 v36, v36, v37
	v_add_f32_e32 v118, v36, v122
	v_cvt_pk_bf16_f32 v36, v38, v39
	v_cvt_pk_bf16_f32 v37, v40, v41
	ds_read_b64_tr_b16 v[154:155], v162 offset:44032
	ds_read_b64_tr_b16 v[156:157], v162 offset:44544
	s_waitcnt lgkmcnt(13)
	v_mfma_f32_32x32x16_bf16 v[82:97], v[130:133], v[110:113], v[82:97]
	v_add_f32_e32 v38, v42, v43
	v_add_f32_e32 v39, v44, v45
	v_add_f32_e32 v38, v38, v39
	v_add_f32_e32 v40, v38, v118
	v_cvt_pk_bf16_f32 v38, v42, v43
	v_cvt_pk_bf16_f32 v39, v44, v45
	ds_read_b64_tr_b16 v[42:43], v162 offset:48128
	ds_read_b64_tr_b16 v[44:45], v162 offset:48640
	s_waitcnt lgkmcnt(14)
	v_mfma_f32_32x32x16_bf16 v[66:81], v[158:161], v[110:113], v[66:81]
	v_add_f32_e32 v41, v46, v47
	v_add_f32_e32 v118, v48, v49
	v_add_f32_e32 v41, v41, v118
	v_add_f32_e32 v166, v41, v40
	v_cvt_pk_bf16_f32 v40, v46, v47
	v_cvt_pk_bf16_f32 v41, v48, v49
	s_waitcnt lgkmcnt(9)
	v_mfma_f32_32x32x16_bf16 v[82:97], v[126:129], v[114:117], v[82:97]
	s_waitcnt lgkmcnt(8)
	v_mfma_f32_32x32x16_bf16 v[66:81], v[134:137], v[114:117], v[66:81]
	s_add_i32 s61, s44, 2
	s_cmp_lt_i32 s61, s71
	s_cselect_b64 s[52:53], -1, 0
	s_cmp_ge_i32 s61, s71
	s_cselect_b64 s[50:51], -1, 0
	s_cbranch_scc1 .LBB0_1322
	s_xor_b32 s54, s99, 0x5000
	s_add_i32 s55, s54, s66
	s_mov_b32 m0, s55
	s_nop 0
	global_load_lds_dwordx4 v[222:223], off
	s_and_b64 vcc, exec, s[42:43]
	s_cbranch_vccnz .LBB0_1322
	s_add_i32 s54, s54, s70
	s_mov_b32 m0, s54
	s_nop 0
	global_load_lds_dwordx4 v[220:221], off
.LBB0_1322:
	s_lshl_b32 s54, s91, 13
	s_add_i32 s54, s54, s72
	s_mov_b32 m0, s54
	s_nop 0
	global_load_lds_dwordx4 v[218:219], off
	s_cmp_lt_i32 s45, s68
	s_cbranch_scc1 .LBB0_1324
	v_add_u32_e32 v47, 0xffffffa5, v195
	v_add_u32_e32 v46, 0xffffff85, v195
	v_cmp_le_i32_e32 vcc, v47, v191
	s_nop 1
	v_cndmask_b32_e32 v66, v230, v66, vcc
	v_cmp_lt_i32_e32 vcc, v46, v191
	s_nop 1
	v_cndmask_b32_e32 v83, v230, v83, vcc
	v_cmp_le_i32_e32 vcc, v46, v191
	v_add_u32_e32 v46, 0xffffffa6, v195
	s_nop 0
	v_cndmask_b32_e32 v82, v230, v82, vcc
	v_cmp_le_i32_e32 vcc, v46, v191
	v_add_u32_e32 v46, 0xffffff87, v195
	s_nop 0
	v_cndmask_b32_e32 v67, v230, v67, vcc
	v_cmp_le_i32_e32 vcc, v46, v191
	v_add_u32_e32 v46, 0xffffffa7, v195
	s_nop 0
	v_cndmask_b32_e32 v84, v230, v84, vcc
	v_cmp_le_i32_e32 vcc, v46, v191
	v_add_u32_e32 v46, 0xffffff88, v195
	s_nop 0
	v_cndmask_b32_e32 v68, v230, v68, vcc
	v_cmp_le_i32_e32 vcc, v46, v191
	v_add_u32_e32 v46, 0xffffffa8, v195
	s_nop 0
	v_cndmask_b32_e32 v85, v230, v85, vcc
	v_cmp_le_i32_e32 vcc, v46, v191
	v_add_u32_e32 v46, 0xffffff8d, v195
	s_nop 0
	v_cndmask_b32_e32 v69, v230, v69, vcc
	v_cmp_le_i32_e32 vcc, v46, v191
	v_add_u32_e32 v46, 0xffffffad, v195
	s_nop 0
	v_cndmask_b32_e32 v86, v230, v86, vcc
	v_cmp_le_i32_e32 vcc, v46, v191
	v_add_u32_e32 v46, 0xffffff8e, v195
	s_nop 0
	v_cndmask_b32_e32 v70, v230, v70, vcc
	v_cmp_le_i32_e32 vcc, v46, v191
	v_add_u32_e32 v46, 0xffffffae, v195
	s_nop 0
	v_cndmask_b32_e32 v87, v230, v87, vcc
	v_cmp_le_i32_e32 vcc, v46, v191
	v_add_u32_e32 v46, 0xffffff8f, v195
	s_nop 0
	v_cndmask_b32_e32 v71, v230, v71, vcc
	v_cmp_le_i32_e32 vcc, v46, v191
	v_add_u32_e32 v46, 0xffffffaf, v195
	s_nop 0
	v_cndmask_b32_e32 v88, v230, v88, vcc
	v_cmp_le_i32_e32 vcc, v46, v191
	v_add_u32_e32 v46, 0xffffff90, v195
	s_nop 0
	v_cndmask_b32_e32 v72, v230, v72, vcc
	v_cmp_le_i32_e32 vcc, v46, v191
	v_add_u32_e32 v46, 0xffffffb0, v195
	s_nop 0
	v_cndmask_b32_e32 v89, v230, v89, vcc
	v_cmp_le_i32_e32 vcc, v46, v191
	v_add_u32_e32 v46, 0xffffff95, v195
	s_nop 0
	v_cndmask_b32_e32 v73, v230, v73, vcc
	v_cmp_le_i32_e32 vcc, v46, v191
	v_add_u32_e32 v46, 0xffffffb5, v195
	s_nop 0
	v_cndmask_b32_e32 v90, v230, v90, vcc
	v_cmp_le_i32_e32 vcc, v46, v191
	v_add_u32_e32 v46, 0xffffff96, v195
	s_nop 0
	v_cndmask_b32_e32 v74, v230, v74, vcc
	v_cmp_le_i32_e32 vcc, v46, v191
	v_add_u32_e32 v46, 0xffffffb6, v195
	s_nop 0
	v_cndmask_b32_e32 v91, v230, v91, vcc
	v_cmp_le_i32_e32 vcc, v46, v191
	v_add_u32_e32 v46, 0xffffff97, v195
	s_nop 0
	v_cndmask_b32_e32 v75, v230, v75, vcc
	v_cmp_le_i32_e32 vcc, v46, v191
	v_add_u32_e32 v46, 0xffffffb7, v195
	s_nop 0
	v_cndmask_b32_e32 v92, v230, v92, vcc
	v_cmp_le_i32_e32 vcc, v46, v191
	v_add_u32_e32 v46, 0xffffff98, v195
	s_nop 0
	v_cndmask_b32_e32 v76, v230, v76, vcc
	v_cmp_le_i32_e32 vcc, v46, v191
	v_add_u32_e32 v46, 0xffffffb8, v195
	s_nop 0
	v_cndmask_b32_e32 v93, v230, v93, vcc
	v_cmp_le_i32_e32 vcc, v46, v191
	v_add_u32_e32 v46, 0xffffff9d, v195
	s_nop 0
	v_cndmask_b32_e32 v77, v230, v77, vcc
	v_cmp_le_i32_e32 vcc, v46, v191
	v_add_u32_e32 v46, 0xffffffbd, v195
	s_nop 0
	v_cndmask_b32_e32 v94, v230, v94, vcc
	v_cmp_le_i32_e32 vcc, v46, v191
	v_add_u32_e32 v46, 0xffffff9e, v195
	s_nop 0
	v_cndmask_b32_e32 v78, v230, v78, vcc
	v_cmp_le_i32_e32 vcc, v46, v191
	v_add_u32_e32 v46, 0xffffffbe, v195
	s_nop 0
	v_cndmask_b32_e32 v95, v230, v95, vcc
	v_cmp_le_i32_e32 vcc, v46, v191
	v_add_u32_e32 v46, 0xffffff9f, v195
	s_nop 0
	v_cndmask_b32_e32 v79, v230, v79, vcc
	v_cmp_le_i32_e32 vcc, v46, v191
	v_add_u32_e32 v46, 0xffffffbf, v195
	s_nop 0
	v_cndmask_b32_e32 v96, v230, v96, vcc
	v_cmp_le_i32_e32 vcc, v46, v191
	v_add_u32_e32 v46, 0xffffffa0, v195
	s_nop 0
	v_cndmask_b32_e32 v80, v230, v80, vcc
	v_cmp_le_i32_e32 vcc, v46, v191
	v_subrev_u32_e32 v46, 64, v195
	s_nop 0
	v_cndmask_b32_e32 v97, v230, v97, vcc
	v_cmp_le_i32_e32 vcc, v46, v191
	s_nop 1
	v_cndmask_b32_e32 v81, v230, v81, vcc
.LBB0_1324:
	v_mfma_f32_32x32x16_bf16 v[2:17], v[138:141], v[142:145], v[2:17]
	v_exp_f32_e32 v82, v82
	v_exp_f32_e32 v83, v83
	v_exp_f32_e32 v84, v84
	v_exp_f32_e32 v85, v85
	v_mfma_f32_32x32x16_bf16 v[18:33], v[138:141], v[146:149], v[18:33]
	v_exp_f32_e32 v86, v86
	v_exp_f32_e32 v87, v87
	v_exp_f32_e32 v88, v88
	v_exp_f32_e32 v89, v89
	v_add_u32_e32 v197, s99, v238
	ds_read_b128 v[138:141], v197
	ds_read_b128 v[130:133], v197 offset:512
	v_mfma_f32_32x32x16_bf16 v[2:17], v[50:53], v[54:57], v[2:17]
	v_exp_f32_e32 v90, v90
	v_exp_f32_e32 v91, v91
	v_exp_f32_e32 v92, v92
	v_exp_f32_e32 v93, v93
	ds_read_b128 v[134:137], v197 offset:2048
	ds_read_b128 v[126:129], v197 offset:2560
	v_mfma_f32_32x32x16_bf16 v[18:33], v[50:53], v[58:61], v[18:33]
	v_exp_f32_e32 v94, v94
	v_exp_f32_e32 v95, v95
	v_exp_f32_e32 v96, v96
	v_exp_f32_e32 v97, v97
	ds_read_b128 v[122:125], v197 offset:4096
	ds_read_b128 v[118:121], v197 offset:4608
	s_waitcnt lgkmcnt(12)
	v_mfma_f32_32x32x16_bf16 v[2:17], v[34:37], v[62:65], v[2:17]
	v_exp_f32_e32 v66, v66
	v_exp_f32_e32 v67, v67
	v_exp_f32_e32 v68, v68
	v_exp_f32_e32 v69, v69
	s_waitcnt lgkmcnt(10)
	v_mfma_f32_32x32x16_bf16 v[18:33], v[34:37], v[150:153], v[18:33]
	v_exp_f32_e32 v70, v70
	v_exp_f32_e32 v71, v71
	v_exp_f32_e32 v72, v72
	v_exp_f32_e32 v73, v73
	s_waitcnt lgkmcnt(8)
	v_mfma_f32_32x32x16_bf16 v[2:17], v[38:41], v[154:157], v[2:17]
	v_exp_f32_e32 v74, v74
	v_exp_f32_e32 v75, v75
	v_exp_f32_e32 v76, v76
	v_exp_f32_e32 v77, v77
	s_waitcnt lgkmcnt(6)
	v_mfma_f32_32x32x16_bf16 v[18:33], v[38:41], v[42:45], v[18:33]
	v_exp_f32_e32 v78, v78
	v_exp_f32_e32 v79, v79
	v_exp_f32_e32 v80, v80
	v_exp_f32_e32 v81, v81
	s_and_b64 s[52:53], s[52:53], exec
	s_cselect_b32 s54, s60, 1
	s_cmp_gt_i32 s54, 2
	s_cbranch_scc1 .Lattn_w3a
	s_cmp_eq_u32 s54, 2
	s_cbranch_scc1 .Lattn_w2a
	s_waitcnt vmcnt(1) lgkmcnt(0)
	s_barrier
	s_branch .LBB0_1331

.LBB0_1331:
	v_mfma_f32_32x32x16_bf16 v[50:65], v[138:141], v[98:101], 0
	v_lshl_add_u32 v199, s92, 13, v240
	ds_read_b64_tr_b16 v[162:163], v199 offset:40960
	ds_read_b64_tr_b16 v[164:165], v199 offset:41472
	s_waitcnt lgkmcnt(7)
	v_add_f32_e32 v34, v82, v83
	v_add_f32_e32 v35, v84, v85
	v_add_f32_e32 v34, v34, v35
	v_cvt_pk_bf16_f32 v154, v82, v83
	v_cvt_pk_bf16_f32 v155, v84, v85
	ds_read_b64_tr_b16 v[158:159], v199 offset:45056
	ds_read_b64_tr_b16 v[160:161], v199 offset:45568
	v_add_f32_e32 v35, v86, v87
	v_add_f32_e32 v36, v88, v89
	v_add_f32_e32 v35, v35, v36
	v_add_f32_e32 v82, v35, v34
	s_waitcnt lgkmcnt(8)
	v_mfma_f32_32x32x16_bf16 v[34:49], v[130:133], v[98:101], 0
	v_cvt_pk_bf16_f32 v156, v86, v87
	v_cvt_pk_bf16_f32 v157, v88, v89
	ds_read_b128 v[170:173], v197 offset:6144
	ds_read_b128 v[174:177], v197 offset:6656
	ds_read_b64_tr_b16 v[150:151], v199 offset:41984
	ds_read_b64_tr_b16 v[152:153], v199 offset:42496
	s_waitcnt lgkmcnt(11)
	v_mfma_f32_32x32x16_bf16 v[50:65], v[134:137], v[102:105], v[50:65]
	v_add_f32_e32 v83, v90, v91
	v_add_f32_e32 v84, v92, v93
	v_add_f32_e32 v83, v83, v84
	v_add_f32_e32 v82, v83, v82
	v_cvt_pk_bf16_f32 v142, v90, v91
	v_cvt_pk_bf16_f32 v143, v92, v93
	ds_read_b64_tr_b16 v[146:147], v199 offset:46080
	ds_read_b64_tr_b16 v[148:149], v199 offset:46592
	s_waitcnt lgkmcnt(12)
	v_mfma_f32_32x32x16_bf16 v[34:49], v[126:129], v[102:105], v[34:49]
	v_add_f32_e32 v83, v94, v95
	v_add_f32_e32 v84, v96, v97
	v_add_f32_e32 v83, v83, v84
	v_add_f32_e32 v82, v83, v82
	v_cvt_pk_bf16_f32 v144, v94, v95
	v_cvt_pk_bf16_f32 v145, v96, v97
	ds_read_b128 v[248:251], v197 offset:8192
	ds_read_b128 v[232:235], v197 offset:8704
	ds_read_b64_tr_b16 v[90:91], v199 offset:43008
	ds_read_b64_tr_b16 v[92:93], v199 offset:43520
	s_waitcnt lgkmcnt(14)
	v_mfma_f32_32x32x16_bf16 v[50:65], v[122:125], v[106:109], v[50:65]
	v_add_f32_e32 v83, v66, v67
	v_add_f32_e32 v84, v68, v69
	v_add_f32_e32 v83, v83, v84
	v_add_f32_e32 v84, v83, v82
	v_cvt_pk_bf16_f32 v82, v66, v67
	v_cvt_pk_bf16_f32 v83, v68, v69
	ds_read_b64_tr_b16 v[86:87], v199 offset:47104
	ds_read_b64_tr_b16 v[88:89], v199 offset:47616
	v_mfma_f32_32x32x16_bf16 v[34:49], v[118:121], v[106:109], v[34:49]
	v_add_f32_e32 v66, v70, v71
	v_add_f32_e32 v67, v72, v73
	v_add_f32_e32 v66, v66, v67
	v_add_f32_e32 v66, v66, v84
	v_cvt_pk_bf16_f32 v84, v70, v71
	v_cvt_pk_bf16_f32 v85, v72, v73
	ds_read_b64_tr_b16 v[70:71], v199 offset:44032
	ds_read_b64_tr_b16 v[72:73], v199 offset:44544
	s_waitcnt lgkmcnt(13)
	v_mfma_f32_32x32x16_bf16 v[50:65], v[170:173], v[110:113], v[50:65]
	v_add_f32_e32 v67, v74, v75
	v_add_f32_e32 v68, v76, v77
	v_add_f32_e32 v67, v67, v68
	v_add_f32_e32 v68, v67, v66
	v_cvt_pk_bf16_f32 v66, v74, v75
	v_cvt_pk_bf16_f32 v67, v76, v77
	ds_read_b64_tr_b16 v[74:75], v199 offset:48128
	ds_read_b64_tr_b16 v[76:77], v199 offset:48640
	s_waitcnt lgkmcnt(14)
	v_mfma_f32_32x32x16_bf16 v[34:49], v[174:177], v[110:113], v[34:49]
	v_add_f32_e32 v69, v78, v79
	v_add_f32_e32 v94, v80, v81
	v_add_f32_e32 v69, v69, v94
	v_add_f32_e32 v94, v69, v68
	v_cvt_pk_bf16_f32 v68, v78, v79
	v_cvt_pk_bf16_f32 v69, v80, v81
	s_waitcnt lgkmcnt(9)
	v_mfma_f32_32x32x16_bf16 v[50:65], v[248:251], v[114:117], v[50:65]
	s_waitcnt lgkmcnt(8)
	v_mfma_f32_32x32x16_bf16 v[34:49], v[232:235], v[114:117], v[34:49]
	s_add_i32 s54, s44, 3
	s_cmp_lt_i32 s54, s71
	s_cselect_b64 s[52:53], -1, 0
	s_cbranch_scc0 .LBB0_1334
	s_ashr_i32 s55, s54, 31
	s_lshl_b64 s[58:59], s[54:55], 17
	v_lshl_add_u64 v[78:79], v[212:213], 0, s[58:59]
	s_add_i32 s58, s98, s66
	s_mov_b32 m0, s58
	s_nop 0
	global_load_lds_dwordx4 v[78:79], off
	s_and_b64 vcc, exec, s[42:43]
	s_cbranch_vccnz .LBB0_1334
	s_lshl_b64 s[54:55], s[54:55], 11
	s_add_i32 s45, s98, s70
	v_lshl_add_u64 v[78:79], v[214:215], 0, s[54:55]
	s_mov_b32 m0, s45
	s_nop 0
	global_load_lds_dwordx4 v[78:79], off
.LBB0_1334:
	s_add_i32 s54, s44, 1
	s_xor_b32 s93, s98, 0x5000
	s_cmp_lt_i32 s54, s71
	s_cselect_b64 s[58:59], -1, 0
	s_cbranch_scc0 .LBB0_1336
	s_ashr_i32 s55, s54, 31
	s_lshl_b64 s[62:63], s[54:55], 17
	s_lshl_b32 s45, s90, 13
	v_lshl_add_u64 v[78:79], v[216:217], 0, s[62:63]
	s_add_i32 s45, s45, s72
	s_mov_b32 m0, s45
	s_nop 0
	global_load_lds_dwordx4 v[78:79], off

.LBB0_1338:
	v_mfma_f32_32x32x16_bf16 v[2:17], v[154:157], v[162:165], v[2:17]
	v_exp_f32_e32 v50, v50
	v_exp_f32_e32 v51, v51
	v_exp_f32_e32 v52, v52
	v_exp_f32_e32 v53, v53
	v_mfma_f32_32x32x16_bf16 v[18:33], v[154:157], v[158:161], v[18:33]
	v_exp_f32_e32 v54, v54
	v_exp_f32_e32 v55, v55
	v_exp_f32_e32 v56, v56
	v_exp_f32_e32 v57, v57
	s_not_b64 s[44:45], s[58:59]
	s_and_b32 s101, s58, 1
	s_andn2_b64 vcc, exec, s[58:59]
	s_cbranch_vccnz .LBB0_1340
	v_add_u32_e32 v79, s93, v238
	ds_read_b128 v[138:141], v79
	ds_read_b128 v[130:133], v79 offset:512
.LBB0_1340:
	v_mfma_f32_32x32x16_bf16 v[2:17], v[142:145], v[150:153], v[2:17]
	v_exp_f32_e32 v58, v58
	v_exp_f32_e32 v59, v59
	v_exp_f32_e32 v60, v60
	v_exp_f32_e32 v61, v61
	s_and_b64 vcc, exec, s[44:45]
	s_cbranch_vccnz .LBB0_1342
	v_add_u32_e32 v79, s93, v238
	ds_read_b128 v[134:137], v79 offset:2048
	ds_read_b128 v[126:129], v79 offset:2560
.LBB0_1342:
	v_mfma_f32_32x32x16_bf16 v[18:33], v[142:145], v[146:149], v[18:33]
	v_exp_f32_e32 v62, v62
	v_exp_f32_e32 v63, v63
	v_exp_f32_e32 v64, v64
	v_exp_f32_e32 v65, v65
	s_and_b64 vcc, exec, s[44:45]
	s_cbranch_vccnz .LBB0_1344
	v_add_u32_e32 v79, s93, v238
	ds_read_b128 v[122:125], v79 offset:4096
	ds_read_b128 v[118:121], v79 offset:4608
.LBB0_1344:
	s_waitcnt lgkmcnt(6)
	v_mfma_f32_32x32x16_bf16 v[2:17], v[82:85], v[90:93], v[2:17]
	v_exp_f32_e32 v34, v34
	v_exp_f32_e32 v35, v35
	v_exp_f32_e32 v36, v36
	v_exp_f32_e32 v37, v37
	s_waitcnt lgkmcnt(4)
	v_mfma_f32_32x32x16_bf16 v[18:33], v[82:85], v[86:89], v[18:33]
	v_exp_f32_e32 v38, v38
	v_exp_f32_e32 v39, v39
	v_exp_f32_e32 v40, v40
	v_exp_f32_e32 v41, v41
	s_waitcnt lgkmcnt(2)
	v_mfma_f32_32x32x16_bf16 v[2:17], v[66:69], v[70:73], v[2:17]
	v_exp_f32_e32 v42, v42
	v_exp_f32_e32 v43, v43
	v_exp_f32_e32 v44, v44
	v_exp_f32_e32 v45, v45
	s_waitcnt lgkmcnt(0)
	v_mfma_f32_32x32x16_bf16 v[18:33], v[66:69], v[74:77], v[18:33]
	v_exp_f32_e32 v46, v46
	v_exp_f32_e32 v47, v47
	v_exp_f32_e32 v48, v48
	v_exp_f32_e32 v49, v49
	s_and_b64 s[44:45], s[52:53], exec
	s_cselect_b32 s58, s69, 0
	s_add_i32 s58, s58, s101
	v_add_f32_e32 v66, v193, v166
	v_add_f32_e32 v193, v66, v94
	v_add_u32_e32 v195, 0x80, v195
	v_lshl_add_u64 v[218:219], v[218:219], 0, s[82:83]
	v_lshl_add_u64 v[220:221], v[220:221], 0, s[96:97]
	v_lshl_add_u64 v[222:223], v[222:223], 0, s[82:83]
	s_mov_b32 s93, s90
	s_mov_b32 s90, s91
	s_mov_b32 s91, s92
	s_mov_b32 s92, s93
	s_xor_b32 s98, s98, 0x5000
	s_xor_b32 s99, s99, 0x5000
	s_mov_b32 s44, s61
	s_and_b64 vcc, exec, s[50:51]
	s_cmp_eq_u32 s58, 3
	s_cbranch_scc1 .Lattn_w3b
	s_cmp_eq_u32 s58, 2
	s_cbranch_scc1 .Lattn_w2b
	s_cmp_eq_u32 s58, 1
	s_cbranch_scc1 .Lattn_w1b
	s_waitcnt vmcnt(0) lgkmcnt(0)
	s_barrier
	s_branch .Lattn_tail
